# conv1r with conversion quota 4 per workgroup in the attention phase
# baseline (speedup 1.0000x reference)
; __device__ __forceinline__ unsigned xb_ld(unsigned* p)              { return __hip_atomic_load(p, __ATOMIC_RELAXED, __HIP_MEMORY_SCOPE_AGENT); }
; __device__ __forceinline__ unsigned xb_add(unsigned* p, unsigned v) { return __hip_atomic_fetch_add(p, v, __ATOMIC_RELAXED, __HIP_MEMORY_SCOPE_AGENT); }
;     ...
;     unsigned ahead = 0xFFFFFFFFu;
;     if (tl == 0 && max_claims > 0) { if (xb_ld(qw) < (unsigned)target) ahead = xb_add(qw, 32u); }
;     for (int nc = 0; nc < max_claims; ++nc) {
;         if (tl == 0) { st[6] = ahead; if (ahead < (unsigned)target && nc + 1 < max_claims) ahead = (ahead + 32u < (unsigned)target) ? xb_add(qw, 32u) : 0xFFFFFFFFu; }
;         __syncthreads();
.LBB0_698:
	s_and_saveexec_b64 s[0:1], s[2:3]
	s_cbranch_execz .LBB0_706
	v_readlane_b32 s14, v254, 27
	s_cmp_lt_u32 s30, 3
	v_cmp_gt_u32_e32 vcc, s25, v129
	v_mov_b32_e32 v139, s14
	s_cselect_b64 s[14:15], -1, 0
	s_and_b64 s[16:17], vcc, s[14:15]
	ds_write_b32 v139, v129
	s_and_saveexec_b64 s[14:15], s[16:17]
	s_cbranch_execz .LBB0_705
	v_cmp_gt_u32_e32 vcc, s27, v129
	v_mov_b32_e32 v129, -1
	s_and_saveexec_b64 s[16:17], vcc
	s_cbranch_execz .LBB0_704
	s_mov_b64 s[20:21], exec
	v_mbcnt_lo_u32_b32 v129, s20, 0
	v_mbcnt_hi_u32_b32 v129, s21, v129
	v_cmp_eq_u32_e32 vcc, 0, v129
	s_and_saveexec_b64 s[18:19], vcc
	s_cbranch_execz .LBB0_703
	s_bcnt1_i32_b64 s20, s[20:21]
	s_lshl_b32 s20, s20, 5
	v_mov_b32_e32 v139, s20
	global_atomic_add v139, v193, v139, s[4:5] sc0

; __device__ __forceinline__ unsigned xb_add(unsigned* p, unsigned v) { return __hip_atomic_fetch_add(p, v, __ATOMIC_RELAXED, __HIP_MEMORY_SCOPE_AGENT); }
;     __device__ __forceinline__ unsigned char* ws() const { return *(unsigned char* const __attribute__((address_space(4)))*)(p + 232); }
;     ...
;     for (int nc = 0; nc < max_claims; ++nc) {
;         if (tl == 0) { st[6] = ahead; if (ahead < (unsigned)target && nc + 1 < max_claims) ahead = (ahead + 32u < (unsigned)target) ? xb_add(qw, 32u) : 0xFFFFFFFFu; }
;         __syncthreads();
;         const unsigned base = st[6];
;         if (base < (unsigned)Q_TOTAL) {
;             const int q0 = (int)base + wave; const bool v0 = q0 < Q_TOTAL, v1 = q0 + 8 < Q_TOTAL, v2 = q0 + 16 < Q_TOTAL, v3 = q0 + 24 < Q_TOTAL;
;             float ta[64], tb[64]; CvtDesc da, db;
;             if (v0) { da = conv_expert_desc(a, ws, q0); cvt_load(da, ta, lane); }
;             if (v1) { db = conv_expert_desc(a, ws, q0 + 8); cvt_load(db, tb, lane); }
;             if (v0) cvt_finish(da, ta, scr, lane);
;             if (v2) { da = conv_expert_desc(a, ws, q0 + 16); cvt_load(da, ta, lane); }
;             if (v1) cvt_finish(db, tb, scr, lane);
;             if (v3) { db = conv_expert_desc(a, ws, q0 + 24); cvt_load(db, tb, lane); }
;             if (v2) cvt_finish(da, ta, scr, lane);
;             if (v3) cvt_finish(db, tb, scr, lane);
;         }
;         if (base >= (unsigned)target) break;
;         __syncthreads();
.LBB0_779:
	s_cmp_ge_u32 s35, s25
	s_mov_b64 s[0:1], -1
	s_cbranch_scc1 .LBB0_697
	s_add_i32 s30, s30, 1
	s_cmp_eq_u32 s30, 4
	s_cselect_b64 s[0:1], -1, 0
	s_barrier
	s_branch .LBB0_697
